# v14 + GLA q/k prefetch + SSD A1/C B-load loops unrolled (4 loads in flight)
# speedup vs baseline: 1.0490x; 1.0012x over previous
.LBB0_674:
	s_or_b64 exec, exec, s[10:11]
	v_add_u32_e32 v10, s8, v74
	s_movk_i32 s0, 0xd00
	v_mul_lo_u32 v34, v10, s0
	s_mov_b32 s0, 0
	v_lshl_add_u64 v[10:11], v[34:35], 1, s[4:5]
	s_mov_b32 s1, 1
	s_mov_b32 s71, s0
	v_lshl_add_u64 v[16:17], v[10:11], 0, s[70:71]
	v_mov_b32_e32 v27, v35
	s_waitcnt lgkmcnt(0)
	v_lshl_add_u64 v[16:17], v[16:17], 0, v[26:27]
	global_load_dwordx2 v[72:73], v[16:17], off offset:256
	global_load_dwordx2 v[90:91], v[16:17], off offset:264
	global_load_dwordx2 v[92:93], v[16:17], off offset:272
	global_load_dwordx2 v[94:95], v[16:17], off offset:280
	ds_read_b32 v29, v75
	s_mov_b64 s[0:1], -1
	s_and_b64 vcc, exec, s[58:59]
	s_cbranch_vccz .LBB0_676
	s_waitcnt lgkmcnt(0)
	v_sub_f32_e32 v27, v29, v70
	s_mov_b64 s[0:1], 0

.LBB0_690:
	v_mov_b64_e32 v[68:69], v[90:91]
	v_mul_f32_e32 v29, 0x3fb8aa3b, v29
	v_exp_f32_e32 v29, v29
	s_waitcnt lgkmcnt(0)
	v_and_b32_e32 v27, 0xffff0000, v73
	s_and_b64 vcc, exec, s[2:3]
	v_mul_f32_e32 v27, v29, v27
	v_cvt_pk_bf16_f32 v27, v27, s0
	ds_write_b16 v89, v27 offset:4416
	ds_read_b32 v27, v75 offset:16
	s_mov_b64 s[0:1], -1
	s_cbranch_vccnz .LBB0_692
	s_waitcnt lgkmcnt(0)
	v_sub_f32_e32 v29, v27, v14
	s_mov_b64 s[0:1], 0

.LBB0_706:
	v_mul_f32_e32 v13, 0x3fb8aa3b, v14
	v_exp_f32_e32 v13, v13
	s_waitcnt lgkmcnt(0)
	v_and_b32_e32 v12, 0xffff0000, v69
	ds_read_b32 v14, v75 offset:32
	s_and_b64 vcc, exec, s[2:3]
	v_mul_f32_e32 v12, v13, v12
	v_cvt_pk_bf16_f32 v12, v12, s0
	ds_write_b16 v89, v12 offset:4736
	v_mov_b64_e32 v[12:13], v[92:93]
	s_mov_b64 s[0:1], -1
	s_cbranch_vccnz .LBB0_708
	s_waitcnt lgkmcnt(1)
	v_sub_f32_e32 v15, v14, v8
	s_mov_b64 s[0:1], 0

.LBB0_722:
	v_mul_f32_e32 v7, 0x3fb8aa3b, v8
	v_exp_f32_e32 v7, v7
	s_waitcnt lgkmcnt(0)
	v_and_b32_e32 v6, 0xffff0000, v13
	ds_read_b32 v8, v75 offset:48
	s_and_b64 vcc, exec, s[2:3]
	v_mul_f32_e32 v6, v7, v6
	v_cvt_pk_bf16_f32 v6, v6, s0
	ds_write_b16 v89, v6 offset:5056
	v_mov_b64_e32 v[6:7], v[94:95]
	s_mov_b64 s[0:1], -1
	s_cbranch_vccnz .LBB0_724
	s_waitcnt lgkmcnt(1)
	v_sub_f32_e32 v9, v8, v4
	s_mov_b64 s[0:1], 0

.LBB0_750:
	v_ashrrev_i32_e32 v6, 5, v3
	v_add_u32_e32 v4, s3, v6
	v_ashrrev_i32_e32 v5, 31, v4
	v_and_b32_e32 v7, 0x7c, v2
	v_lshlrev_b64 v[4:5], 11, v[4:5]
	v_lshlrev_b32_e32 v34, 1, v7
	v_lshl_add_u64 v[4:5], s[0:1], 0, v[4:5]
	v_lshl_add_u64 v[4:5], v[4:5], 0, v[34:35]
	s_mov_b64 s[14:15], 0x8000
	global_load_dwordx2 v[96:97], v[4:5], off offset:1024
	v_lshl_add_u64 v[4:5], v[4:5], 0, s[14:15]
	global_load_dwordx2 v[98:99], v[4:5], off offset:1024
	v_lshl_add_u64 v[4:5], v[4:5], 0, s[14:15]
	global_load_dwordx2 v[100:101], v[4:5], off offset:1024
	v_lshl_add_u64 v[4:5], v[4:5], 0, s[14:15]
	global_load_dwordx2 v[102:103], v[4:5], off offset:1024
	v_lshlrev_b32_e32 v6, 1, v6
	v_mul_u32_u24_e32 v7, 0x90, v7
	v_add3_u32 v6, 0, v6, v7
	s_waitcnt vmcnt(0)
	v_lshlrev_b32_e32 v7, 16, v96
	v_and_b32_e32 v4, 0xffff0000, v96
	v_lshlrev_b32_e32 v8, 16, v97
	v_and_b32_e32 v5, 0xffff0000, v97
	v_cvt_pk_bf16_f32 v7, v7, s0
	v_cvt_pk_bf16_f32 v4, v4, s0
	v_cvt_pk_bf16_f32 v8, v8, s0
	v_cvt_pk_bf16_f32 v5, v5, s0
	ds_write_b16 v6, v7
	ds_write_b16 v6, v4 offset:144
	ds_write_b16 v6, v8 offset:288
	ds_write_b16 v6, v5 offset:432
	v_lshlrev_b32_e32 v7, 16, v98
	v_and_b32_e32 v4, 0xffff0000, v98
	v_lshlrev_b32_e32 v8, 16, v99
	v_and_b32_e32 v5, 0xffff0000, v99
	v_cvt_pk_bf16_f32 v7, v7, s0
	v_cvt_pk_bf16_f32 v4, v4, s0
	v_cvt_pk_bf16_f32 v8, v8, s0
	v_cvt_pk_bf16_f32 v5, v5, s0
	ds_write_b16 v6, v7 offset:32
	ds_write_b16 v6, v4 offset:176
	ds_write_b16 v6, v8 offset:320
	ds_write_b16 v6, v5 offset:464
	v_lshlrev_b32_e32 v7, 16, v100
	v_and_b32_e32 v4, 0xffff0000, v100
	v_lshlrev_b32_e32 v8, 16, v101
	v_and_b32_e32 v5, 0xffff0000, v101
	v_cvt_pk_bf16_f32 v7, v7, s0
	v_cvt_pk_bf16_f32 v4, v4, s0
	v_cvt_pk_bf16_f32 v8, v8, s0
	v_cvt_pk_bf16_f32 v5, v5, s0
	ds_write_b16 v6, v7 offset:64
	ds_write_b16 v6, v4 offset:208
	ds_write_b16 v6, v8 offset:352
	ds_write_b16 v6, v5 offset:496
	v_lshlrev_b32_e32 v7, 16, v102
	v_and_b32_e32 v4, 0xffff0000, v102
	v_lshlrev_b32_e32 v8, 16, v103
	v_and_b32_e32 v5, 0xffff0000, v103
	v_cvt_pk_bf16_f32 v7, v7, s0
	v_cvt_pk_bf16_f32 v4, v4, s0
	v_cvt_pk_bf16_f32 v8, v8, s0
	v_cvt_pk_bf16_f32 v5, v5, s0
	ds_write_b16 v6, v7 offset:96
	ds_write_b16 v6, v4 offset:240
	ds_write_b16 v6, v8 offset:384
	ds_write_b16 v6, v5 offset:528

.LBB0_948:
	s_or_b64 exec, exec, s[8:9]
	v_add_u32_e32 v10, s18, v136
	s_movk_i32 s0, 0xd00
	v_mul_lo_u32 v34, v10, s0
	s_mov_b32 s0, 0
	v_lshl_add_u64 v[10:11], v[34:35], 1, s[4:5]
	s_mov_b32 s1, 1
	s_mov_b32 s83, s0
	v_lshl_add_u64 v[16:17], v[10:11], 0, s[82:83]
	v_mov_b32_e32 v155, v35
	s_waitcnt lgkmcnt(0)
	v_lshl_add_u64 v[16:17], v[16:17], 0, v[154:155]
	global_load_dwordx2 v[24:25], v[16:17], off
	global_load_dwordx2 v[22:23], v[16:17], off offset:256
	global_load_dwordx2 v[238:239], v[16:17], off offset:8
	global_load_dwordx2 v[240:241], v[16:17], off offset:264
	global_load_dwordx2 v[242:243], v[16:17], off offset:16
	global_load_dwordx2 v[244:245], v[16:17], off offset:272
	global_load_dwordx2 v[246:247], v[16:17], off offset:24
	global_load_dwordx2 v[248:249], v[16:17], off offset:280
	ds_read_b32 v26, v172
	ds_read_b32 v28, v174 offset:1980
	s_mov_b64 s[0:1], -1
	s_and_b64 vcc, exec, s[74:75]
	s_cbranch_vccz .LBB0_950
	s_waitcnt lgkmcnt(1)
	v_sub_f32_e32 v20, v26, v20
	s_waitcnt lgkmcnt(0)
	v_sub_f32_e32 v27, v28, v20
	v_mul_f32_e32 v27, 0x3fb8aa3b, v27
	v_exp_f32_e32 v27, v27
	v_sub_f32_e32 v29, v20, v28
	s_mov_b64 s[0:1], 0

.LBB0_964:
	s_waitcnt lgkmcnt(1)
	v_mul_f32_e32 v20, 0x3fb8aa3b, v22
	v_and_b32_e32 v18, 0xffff0000, v25
	v_exp_f32_e32 v20, v20
	v_mul_f32_e32 v18, 0x3e3504f3, v18
	v_mul_f32_e32 v18, v18, v21
	v_and_b32_e32 v19, 0xffff0000, v23
	v_cvt_pk_bf16_f32 v18, v18, s0
	ds_write_b16 v175, v18 offset:4262
	v_mul_f32_e32 v18, v20, v19
	v_cvt_pk_bf16_f32 v18, v18, s0
	ds_write_b16 v175, v18 offset:6822
	v_mov_b64_e32 v[20:21], v[238:239]
	v_mov_b64_e32 v[18:19], v[240:241]
	ds_read_b32 v22, v172 offset:16
	ds_read_b32 v23, v174 offset:1996
	s_mov_b64 s[0:1], -1
	s_and_b64 vcc, exec, s[2:3]
	s_cbranch_vccnz .LBB0_966
	s_waitcnt lgkmcnt(1)
	v_sub_f32_e32 v14, v22, v14
	s_waitcnt lgkmcnt(0)
	v_sub_f32_e32 v24, v23, v14
	v_mul_f32_e32 v24, 0x3fb8aa3b, v24
	v_exp_f32_e32 v24, v24
	v_sub_f32_e32 v25, v14, v23
	s_mov_b64 s[0:1], 0

.LBB0_980:
	s_waitcnt lgkmcnt(1)
	v_mul_f32_e32 v14, 0x3fb8aa3b, v18
	v_and_b32_e32 v12, 0xffff0000, v21
	v_exp_f32_e32 v14, v14
	v_mul_f32_e32 v12, 0x3e3504f3, v12
	v_mul_f32_e32 v12, v12, v15
	v_and_b32_e32 v13, 0xffff0000, v19
	v_cvt_pk_bf16_f32 v12, v12, s0
	ds_write_b16 v175, v12 offset:4270
	v_mul_f32_e32 v12, v14, v13
	v_cvt_pk_bf16_f32 v12, v12, s0
	ds_write_b16 v175, v12 offset:6830
	v_mov_b64_e32 v[14:15], v[242:243]
	v_mov_b64_e32 v[12:13], v[244:245]
	ds_read_b32 v18, v172 offset:32
	ds_read_b32 v19, v174 offset:2012
	s_mov_b64 s[0:1], -1
	s_and_b64 vcc, exec, s[2:3]
	s_cbranch_vccnz .LBB0_982
	s_waitcnt lgkmcnt(1)
	v_sub_f32_e32 v8, v18, v8
	s_waitcnt lgkmcnt(0)
	v_sub_f32_e32 v20, v19, v8
	v_mul_f32_e32 v20, 0x3fb8aa3b, v20
	v_exp_f32_e32 v20, v20
	v_sub_f32_e32 v21, v8, v19
	s_mov_b64 s[0:1], 0

.LBB0_996:
	s_waitcnt lgkmcnt(1)
	v_mul_f32_e32 v8, 0x3fb8aa3b, v12
	v_and_b32_e32 v6, 0xffff0000, v15
	v_exp_f32_e32 v8, v8
	v_mul_f32_e32 v6, 0x3e3504f3, v6
	v_mul_f32_e32 v6, v6, v9
	v_and_b32_e32 v7, 0xffff0000, v13
	v_cvt_pk_bf16_f32 v6, v6, s0
	ds_write_b16 v175, v6 offset:4278
	v_mul_f32_e32 v6, v8, v7
	v_cvt_pk_bf16_f32 v6, v6, s0
	ds_write_b16 v175, v6 offset:6838
	v_mov_b64_e32 v[8:9], v[246:247]
	v_mov_b64_e32 v[6:7], v[248:249]
	ds_read_b32 v12, v172 offset:48
	ds_read_b32 v13, v174 offset:2028
	s_mov_b64 s[0:1], -1
	s_and_b64 vcc, exec, s[2:3]
	s_cbranch_vccnz .LBB0_998
	s_waitcnt lgkmcnt(1)
	v_sub_f32_e32 v4, v12, v4
	s_waitcnt lgkmcnt(0)
	v_sub_f32_e32 v14, v13, v4
	v_mul_f32_e32 v14, 0x3fb8aa3b, v14
	v_exp_f32_e32 v14, v14
	v_sub_f32_e32 v15, v4, v13
	s_mov_b64 s[0:1], 0

.LBB0_1019:
	v_ashrrev_i32_e32 v8, 5, v3
	v_add_u32_e32 v4, s2, v8
	v_ashrrev_i32_e32 v5, 31, v4
	v_lshlrev_b64 v[4:5], 11, v[4:5]
	v_lshlrev_b32_e32 v6, 1, v2
	v_lshl_add_u64 v[4:5], s[14:15], 0, v[4:5]
	v_and_b32_e32 v34, 0xf8, v6
	v_lshl_add_u64 v[4:5], v[4:5], 0, v[34:35]
	s_mov_b64 s[18:19], 0x8000
	global_load_dwordx2 v[238:239], v[4:5], off offset:1024
	global_load_dwordx2 v[240:241], v[4:5], off offset:1536
	v_lshl_add_u64 v[4:5], v[4:5], 0, s[18:19]
	global_load_dwordx2 v[242:243], v[4:5], off offset:1024
	global_load_dwordx2 v[244:245], v[4:5], off offset:1536
	v_lshl_add_u64 v[4:5], v[4:5], 0, s[18:19]
	global_load_dwordx2 v[246:247], v[4:5], off offset:1024
	global_load_dwordx2 v[248:249], v[4:5], off offset:1536
	v_lshl_add_u64 v[4:5], v[4:5], 0, s[18:19]
	global_load_dwordx2 v[198:199], v[4:5], off offset:1024
	global_load_dwordx2 v[208:209], v[4:5], off offset:1536
	v_mul_lo_u32 v8, v8, s83
	s_lshl_b32 s18, s83, 4
	v_add3_u32 v8, 0, v8, v34
	s_waitcnt vmcnt(0)
	v_lshlrev_b32_e32 v9, 16, v238
	v_and_b32_e32 v6, 0xffff0000, v238
	v_lshlrev_b32_e32 v10, 16, v239
	v_and_b32_e32 v7, 0xffff0000, v239
	v_lshlrev_b32_e32 v11, 16, v240
	v_and_b32_e32 v12, 0xffff0000, v240
	v_lshlrev_b32_e32 v13, 16, v241
	v_and_b32_e32 v14, 0xffff0000, v241
	v_cvt_pk_bf16_f32 v4, v9, v6
	v_cvt_pk_bf16_f32 v5, v10, v7
	v_cvt_pk_bf16_f32 v6, v11, v12
	v_cvt_pk_bf16_f32 v7, v13, v14
	ds_write2st64_b64 v8, v[6:7], v[4:5] offset1:34
	v_add_u32_e32 v8, s18, v8
	v_lshlrev_b32_e32 v9, 16, v242
	v_and_b32_e32 v6, 0xffff0000, v242
	v_lshlrev_b32_e32 v10, 16, v243
	v_and_b32_e32 v7, 0xffff0000, v243
	v_lshlrev_b32_e32 v11, 16, v244
	v_and_b32_e32 v12, 0xffff0000, v244
	v_lshlrev_b32_e32 v13, 16, v245
	v_and_b32_e32 v14, 0xffff0000, v245
	v_cvt_pk_bf16_f32 v4, v9, v6
	v_cvt_pk_bf16_f32 v5, v10, v7
	v_cvt_pk_bf16_f32 v6, v11, v12
	v_cvt_pk_bf16_f32 v7, v13, v14
	ds_write2st64_b64 v8, v[6:7], v[4:5] offset1:34
	v_add_u32_e32 v8, s18, v8
	v_lshlrev_b32_e32 v9, 16, v246
	v_and_b32_e32 v6, 0xffff0000, v246
	v_lshlrev_b32_e32 v10, 16, v247
	v_and_b32_e32 v7, 0xffff0000, v247
	v_lshlrev_b32_e32 v11, 16, v248
	v_and_b32_e32 v12, 0xffff0000, v248
	v_lshlrev_b32_e32 v13, 16, v249
	v_and_b32_e32 v14, 0xffff0000, v249
	v_cvt_pk_bf16_f32 v4, v9, v6
	v_cvt_pk_bf16_f32 v5, v10, v7
	v_cvt_pk_bf16_f32 v6, v11, v12
	v_cvt_pk_bf16_f32 v7, v13, v14
	ds_write2st64_b64 v8, v[6:7], v[4:5] offset1:34
	v_add_u32_e32 v8, s18, v8
	v_lshlrev_b32_e32 v9, 16, v198
	v_and_b32_e32 v6, 0xffff0000, v198
	v_lshlrev_b32_e32 v10, 16, v199
	v_and_b32_e32 v7, 0xffff0000, v199
	v_lshlrev_b32_e32 v11, 16, v208
	v_and_b32_e32 v12, 0xffff0000, v208
	v_lshlrev_b32_e32 v13, 16, v209
	v_and_b32_e32 v14, 0xffff0000, v209
	v_cvt_pk_bf16_f32 v4, v9, v6
	v_cvt_pk_bf16_f32 v5, v10, v7
	v_cvt_pk_bf16_f32 v6, v11, v12
	v_cvt_pk_bf16_f32 v7, v13, v14
	ds_write2st64_b64 v8, v[6:7], v[4:5] offset1:34
